# P7: each conversion class of an XCD takes 16 contiguous GEMM units (unit index permuted within the XCD; class function and everything else unchanged) for better L2 panel sharing
# speedup vs baseline: 1.0023x; 1.0023x over previous
; #define SEAM(k) do { if (IN(k) && IN((k) + 1)) xcd_barrier(bar); if (PROBE_PHASE == (k)) pr_dt = __builtin_amdgcn_s_memrealtime() - pr_t0; if (PROBE_PHASE == (k) + 1) pr_t0 = __builtin_amdgcn_s_memrealtime(); } while (0)
; template <class Epi, class Sched, bool MOE>
; __device__ __forceinline__ void gemm_rounds(const Frame& F, const Args& a, Sched& S, const Epi& E, int gbase, int nominal_rounds, int slab_base) {
;     unsigned* ctl = (unsigned*)(a.ws + WS_CTL);
;     int i = 0;
;     for (;;) {
;         pg8::Unit u; S.lo = 0; S.hi = 1 << 20;
;         if (!S.next(i, u)) break;
;         const int g = gbase + i, ph = (g + F.vcu) % 2;
; __global__ void __launch_bounds__(NT, 2) mk_fwd(Args args) {
;     ...
;     if (IN(7)) { moe_tables(F, args, 16);
;         pg8::MoeOrder<true> So{(const char*)(ws + WS_H2), (const char*)(ws + WS_WGU), (const int*)(ws + WS_TOKOF), T + L_CNT, T + L_PFXU, T + L_POFF, 16, F.G, F.vcu, 0, 1 << 20};
;         pg8::EpiGU E{(unsigned char*)(ws + WS_ACT), args.in[14], T + L_POFF};
;         const int R1 = (__builtin_amdgcn_readfirstlane(T[L_PFXU + NE]) + F.G - 1) / F.G;
;         gemm_rounds<pg8::EpiGU, pg8::MoeOrder<true>, true>(F, args, So, E, 3, R1, 0); } SEAM(7);
.LBB0_766:
	s_add_u32 s18, s74, 0x45e02000
	s_addc_u32 s19, s75, 0
	s_add_u32 s81, s74, 0x2100000
	s_addc_u32 s82, s75, 0
	s_add_u32 s83, s74, 0x47e02000
	s_addc_u32 s86, s75, 0
	s_add_u32 s20, s74, 0x47f62000
	s_addc_u32 s21, s75, 0
	s_add_i32 s0, 0, 0x20280
	v_mov_b32_e32 v1, s0
	s_waitcnt lgkmcnt(0)
	s_barrier
	ds_read_b32 v1, v1
	s_abs_i32 s1, s33
	v_cvt_f32_u32_e32 v2, s1
	v_writelane_b32 v252, s34, 6
	v_mov_b32_e32 v195, 0
	s_waitcnt lgkmcnt(0)
	v_readfirstlane_b32 s0, v1
	v_rcp_iflag_f32_e32 v1, v2
	s_add_i32 s0, s33, s0
	s_add_i32 s0, s0, -1
	v_writelane_b32 v252, s35, 7
	v_mul_f32_e32 v1, 0x4f7ffffe, v1
	v_cvt_u32_f32_e32 v1, v1
	s_ashr_i32 s2, s0, 31
	v_writelane_b32 v252, s2, 10
	s_ashr_i32 s2, s33, 31
	v_writelane_b32 v252, s2, 14
	s_abs_i32 s2, s0
	v_writelane_b32 v252, s1, 8
	s_sub_i32 s0, 0, s1
	v_readfirstlane_b32 s1, v1
	s_mul_i32 s0, s0, s1
	s_mul_hi_u32 s0, s1, s0
	s_add_i32 s1, s1, s0
	v_writelane_b32 v252, s2, 12
	s_mul_hi_u32 s0, s2, s1
	v_writelane_b32 v252, s0, 16
	s_lshr_b32 s0, s33, 31
	v_readlane_b32 s1, v253, 5
	s_and_b32 s98, s1, 31
	s_lshr_b32 s99, s98, 1
	s_and_b32 s98, s98, 1
	s_lshl_b32 s98, s98, 4
	s_or_b32 s98, s98, s99
	s_andn2_b32 s99, s1, 31
	s_or_b32 s98, s98, s99
	v_writelane_b32 v252, s98, 50
	s_add_i32 s0, s33, s0
	s_add_i32 s54, s1, 3
	s_ashr_i32 s0, s0, 1
	s_cmp_lt_i32 s1, s0
	s_cselect_b64 s[10:11], -1, 0
	s_add_u32 s52, s74, 0xc000
	s_addc_u32 s53, s75, 0
	s_lshl_b32 s76, s1, 3
	s_add_i32 s76, s76, s95
	v_writelane_b32 v253, s0, 36
	s_lshl_b32 s0, s95, 14
	s_ashr_i32 s4, s76, 10
	s_add_i32 s80, s0, 0
	s_add_i32 s0, s4, 2
	v_writelane_b32 v252, s0, 0
	s_add_i32 s0, s4, 4
	v_writelane_b32 v252, s0, 18
	s_and_b32 s0, s76, 0xffffff80
	v_writelane_b32 v253, s0, 6
	s_lshl_b32 s0, s76, 5
	s_and_b32 s2, s0, 0xfe0
	s_lshl_b32 s0, s76, 16
	s_and_b32 s0, s0, 0x7f0000
	s_ashr_i32 s5, s4, 31
	s_bfe_u32 s39, s76, 0x40006
	s_ashr_i32 s77, s76, 7
	v_writelane_b32 v253, s0, 40
	s_lshl_b64 s[0:1], s[4:5], 24
	s_add_u32 s0, s50, s0
	s_addc_u32 s1, s51, s1
	v_writelane_b32 v252, s0, 2
	v_mbcnt_lo_u32_b32 v1, -1, 0
	s_mov_b32 s90, 0x5010400
	v_writelane_b32 v252, s1, 3
	s_lshl_b64 s[0:1], s[4:5], 22
	s_add_u32 s0, s74, s0
	s_addc_u32 s1, s75, s1
	s_add_u32 s0, s0, 0x22100000
	s_addc_u32 s1, s1, 0
	v_writelane_b32 v253, s0, 62
	s_mov_b32 s89, 0x7030602
	s_mov_b32 s15, 0x5040100
	v_writelane_b32 v253, s1, 63
	s_sub_i32 s0, s4, 60
	v_writelane_b32 v252, s0, 4
	s_add_u32 s0, s74, 0x45e02080
	s_addc_u32 s1, s75, 0
	v_writelane_b32 v253, s0, 50
	s_add_i32 s55, 0, 0x20048
	s_add_i32 s56, 0, 0x2004c
	v_writelane_b32 v253, s1, 51
	s_mov_b32 s0, s4
	v_writelane_b32 v253, s0, 44
	s_add_i32 s57, 0, 0x20050
	s_add_i32 s97, 0, 0x20200
	v_writelane_b32 v253, s1, 45
	s_add_i32 s0, s4, 8
	v_writelane_b32 v252, s0, 20
	s_lshl_b32 s0, s2, 2
	v_writelane_b32 v253, s0, 42
	s_mov_b32 s78, 0x7060302
	s_mov_b32 s7, 0x20000
	v_writelane_b32 v253, s1, 43
	s_add_i32 s0, 0, 0x22000
	v_writelane_b32 v253, s0, 34
	s_add_i32 s0, 0, 0x22200
	v_writelane_b32 v253, s0, 30
	v_writelane_b32 v253, s52, 46
	s_add_i32 s58, 0, 0x20044
	s_mov_b32 s8, 0x40000
	v_writelane_b32 v253, s53, 47
	v_writelane_b32 v253, s54, 48
	v_writelane_b32 v253, s55, 52
	v_writelane_b32 v253, s56, 54
	s_mov_b32 s6, 0x800000
	v_mov_b32_e32 v198, 1
	v_mov_b32_e32 v199, 0x7f
	v_mbcnt_hi_u32_b32 v1, -1, v1
	v_mov_b64_e32 v[196:197], 0x1e8481
	v_mov_b32_e32 v200, 0x41000000
	s_mov_b32 s23, 0xc0c00000
	s_mov_b32 s25, 0
	s_mov_b32 s37, 0
	s_mov_b32 s38, 0x3c800000
	v_writelane_b32 v253, s57, 38
	v_writelane_b32 v253, s58, 32
	s_branch .LBB0_769

; __device__ __forceinline__ int fresh_lane() { int l = (int)__builtin_amdgcn_mbcnt_hi(~0u, __builtin_amdgcn_mbcnt_lo(~0u, 0u)); asm volatile("" : "+v"(l)); return l; }
;     __device__ __forceinline__ bool next(int i, Unit& u) const {
;         if (i >= hi) return false;
;         const int L = i * G + c;
;         const unsigned msk = (unsigned)__ballot(L < pfxU[(fresh_lane() & 31) + 1]);
;         if (msk == 0u) return false;
;         const int e = __builtin_ctz(msk);
;         const int r = L - __builtin_amdgcn_readfirstlane(pfxU[e]), mt = (__builtin_amdgcn_readfirstlane(cnt[e]) + 255) >> 8;
;         u.e = e; u.pn = r / mt; u.pm = r - u.pn * mt; return true;
; template <class Epi, class Sched, bool MOE>
; __device__ __forceinline__ void gemm_rounds(const Frame& F, const Args& a, Sched& S, const Epi& E, int gbase, int nominal_rounds, int slab_base) {
;     ...
;     for (;;) {
;         pg8::Unit u; S.lo = 0; S.hi = 1 << 20;
;         if (!S.next(i, u)) break;
;         const int g = gbase + i, ph = (g + F.vcu) % 2;
.LBB0_769:
	s_cmp_gt_i32 s25, 0xfffff
	s_mov_b64 s[0:1], 0
	s_cbranch_scc1 .LBB0_771
	v_mov_b32_e32 v2, v1
	s_mul_i32 s0, s25, s33
	v_and_b32_e32 v2, 31, v2
	v_lshl_add_u32 v2, v2, 2, s97
	ds_read_b32 v2, v2 offset:4
	v_readlane_b32 s1, v252, 50
	s_add_i32 s0, s0, s1
	s_waitcnt lgkmcnt(0)
	v_cmp_lt_i32_e32 vcc, s0, v2
	s_cmp_lg_u32 vcc_lo, 0
	s_cselect_b64 s[0:1], -1, 0
	s_ff1_i32_b32 s4, vcc_lo
	s_and_b64 s[2:3], s[0:1], exec
	s_cselect_b32 s9, s4, s9

; #define LAS __attribute__((address_space(3)))
; template <class Epi, class Sched, bool MOE>
; __device__ __forceinline__ void gemm_rounds(const Frame& F, const Args& a, Sched& S, const Epi& E, int gbase, int nominal_rounds, int slab_base) {
;     ...
;         const bool more = __builtin_amdgcn_readfirstlane(((volatile LAS int*)(F.lds + LDSCTL_OFF))[L_BGDONE]) < 64;
;         const int j = more ? i + 2 - ph : (1 << 20);
;         if (MOE) { int elast = u.e; for (int q = i + 1; q < j; ++q) { pg8::Unit t2; if (!S.next(q, t2)) break; elast = t2.e; } bg_wait_slab(F, a, slab_base + elast); }
.LBB0_887:
	s_waitcnt vmcnt(0)
	v_mov_b32_e32 v2, s57
	ds_read_b32 v2, v2
	s_waitcnt lgkmcnt(0)
	v_readfirstlane_b32 s0, v2
	s_cmp_gt_i32 s0, 63
	s_cselect_b64 s[34:35], -1, 0
	s_sub_i32 s1, s25, s14
	s_add_i32 s93, s1, 2
	s_cmp_lt_i32 s0, 64
	s_cselect_b32 s87, s93, 0x100000
	s_add_i32 s4, s25, 1
	s_cmp_ge_i32 s4, s87
	s_cbranch_scc1 .LBB0_894
	s_mul_i32 s0, s33, s4
	v_readlane_b32 s1, v252, 50
	s_add_i32 s5, s1, s0
	s_mov_b32 s14, s9
	s_cmp_gt_i32 s4, 0xfffff
	s_mov_b64 s[2:3], 0
	s_cbranch_scc0 .LBB0_891

;     __device__ __forceinline__ const char* a_base(const Unit& u) const { return GATHER ? A : A + ((size_t)__builtin_amdgcn_readfirstlane(poff[u.e]) + (size_t)u.pm * BM) * ROWB; }
; #define PG8_STAGE_A(bufoff, gbase, h) do { _Pragma("unroll") for (int _i = 0; _i < 2; ++_i) PG8_GLDS(gbase, va[(h) * 2 + _i], ldsb + (bufoff) + ldsw + _i * 8192); } while (0)
;     __device__ __forceinline__ void a_offs(const Unit& u, const unsigned (&nat)[2], unsigned (&v)[4]) const {
;         if (!GATHER) { v[0] = nat[0]; v[1] = nat[1]; v[2] = nat[0] + Geo<true>::HSTEP; v[3] = nat[1] + Geo<true>::HSTEP; return; }
;         const int n = cnt[u.e];
;         unsigned off[4]; int tok[4];
; #pragma unroll
;         for (int h = 0; h < 2; ++h)
; #pragma unroll
;             for (int i = 0; i < 2; ++i) { int pos = u.pm * BM + h * HALF + (int)(nat[i] / ROWB); pos = pos < n ? pos : n - 1; off[h * 2 + i] = (unsigned)pos * 4u; }
;         asm volatile("global_load_dword %0, %4, %8\n\tglobal_load_dword %1, %5, %8\n\tglobal_load_dword %2, %6, %8\n\tglobal_load_dword %3, %7, %8\n\ts_waitcnt vmcnt(0)"
;                      : "=&v"(tok[0]), "=&v"(tok[1]), "=&v"(tok[2]), "=&v"(tok[3]) : "v"(off[0]), "v"(off[1]), "v"(off[2]), "v"(off[3]), "s"(tokof + (size_t)u.e * ECAP) : "memory");
; #pragma unroll
;         for (int q = 0; q < 4; ++q) v[q] = (unsigned)tok[q] * ROWB + nat[q & 1] % ROWB;
; template <class Epi, class Sched>
; __device__ __forceinline__ void gemm_phase(LAS unsigned char* lds, const Sched& S, const Epi& E) {
;     ...
;     Unit cur, nxt; int ui = S.lo;
;     if (!S.next(ui, cur)) return;
;     f32x4 acc[2][2][4][2];
; #pragma unroll
;     for (int a = 0; a < 2; ++a)
; #pragma unroll
;         for (int b = 0; b < 2; ++b)
; #pragma unroll
;             for (int m = 0; m < 4; ++m)
; #pragma unroll
;                 for (int n = 0; n < 2; ++n) acc[a][b][m][n] = (f32x4){0.f, 0.f, 0.f, 0.f};
;     i32x4 At[4][2], B0[2][2], B1[2][2];
;     unsigned va[4]; S.a_offs(cur, natA, va);
;     const char* cA = S.a_base(cur); const char* cB = S.b_base(cur);
;     PG8_STAGE_B(PG8_SB(0, 0), cB); PG8_STAGE_B(PG8_SB(0, 1), cB + HSTEP); PG8_STAGE_A(PG8_SA(0, 0), cA, 0); PG8_STAGE_A(PG8_SA(0, 1), cA, 1);
;     if (wr == 1) PG8_BAR;
;     PG8_WAIT_V(2); PG8_BAR;
;     PG8_STAGE_B(PG8_SB(1, 0), cB + kstep); PG8_STAGE_A(PG8_SA(1, 0), cA + kstep, 0); PG8_STAGE_B(PG8_SB(1, 1), cB + HSTEP + kstep);
.LBB0_995:
	v_readfirstlane_b32 s2, v0
	v_mov_b32_e32 v2, v1
	s_cmp_ge_i32 s25, s87
	s_cbranch_scc1 .LBB0_768
	v_mov_b32_e32 v3, v1
	s_mul_i32 s0, s25, s33
	v_and_b32_e32 v3, 31, v3
	v_lshl_add_u32 v3, v3, 2, s97
	ds_read_b32 v3, v3 offset:4
	v_readlane_b32 s1, v252, 50
	s_add_i32 s0, s0, s1
	s_waitcnt lgkmcnt(0)
	v_cmp_lt_i32_e32 vcc, s0, v3
	s_cmp_eq_u32 vcc_lo, 0
	s_cbranch_scc1 .LBB0_768
	s_and_b32 s1, s2, 0xffffffc0
	v_add_u32_e32 v3, s1, v2
	v_ashrrev_i32_e32 v5, 31, v3
	v_lshrrev_b32_e32 v5, 26, v5
	v_lshlrev_b32_e32 v4, 4, v3
	v_add_u32_e32 v5, v3, v5
	v_bfe_i32 v3, v3, 27, 1
	v_lshrrev_b32_e32 v3, 22, v3
	v_add_u32_e32 v3, v4, v3
	v_and_b32_e32 v3, 0xfffffc00, v3
	v_sub_u32_e32 v3, v4, v3
	v_lshrrev_b32_e32 v6, 4, v3
	v_bitop3_b32 v3, v6, v3, 32 bitop3:0x6c
	v_ashrrev_i32_e32 v7, 31, v3
	v_lshrrev_b32_e32 v7, 26, v7
	v_ashrrev_i32_e32 v5, 6, v5
	v_add_u32_e32 v7, v3, v7
	v_lshlrev_b32_e32 v6, 3, v5
	v_ashrrev_i32_e32 v8, 6, v7
	v_and_b32_e32 v7, 0xc0, v7
	v_and_b32_e32 v6, -16, v6
	v_lshlrev_b32_e32 v5, 5, v5
	v_sub_u32_e32 v3, v3, v7
	v_add_u32_e32 v6, v8, v6
	v_and_b32_e32 v5, 32, v5
	v_ashrrev_i16_sdwa v3, v198, sext(v3) dst_sel:DWORD dst_unused:UNUSED_PAD src0_sel:DWORD src1_sel:BYTE_0
	v_add_u32_sdwa v3, v5, sext(v3) dst_sel:DWORD dst_unused:UNUSED_PAD src0_sel:DWORD src1_sel:WORD_0
	v_lshlrev_b32_e32 v5, 1, v6
	v_lshrrev_b32_e32 v7, 2, v6
	v_and_b32_e32 v8, 3, v8
	s_mov_b32 s1, 0x1fffe0
	v_and_b32_e32 v5, 24, v5
	v_and_b32_e32 v7, 4, v7
	v_and_or_b32 v8, v6, s1, v8
	v_or3_b32 v5, v8, v7, v5
	v_lshlrev_b32_e32 v7, 1, v3
	v_add_u32_e32 v4, 0x2000, v4
	v_lshl_add_u32 v194, v5, 11, v7
	v_ashrrev_i32_e32 v5, 31, v4
	v_lshrrev_b32_e32 v5, 22, v5
	v_add_u32_e32 v5, v4, v5
	v_ashrrev_i32_e32 v5, 10, v5
	v_mul_i32_i24_e32 v8, 0x400, v5
	v_sub_u32_e32 v4, v4, v8
	v_lshrrev_b32_e32 v8, 4, v4
	v_bitop3_b32 v4, v8, v4, 32 bitop3:0x6c
	v_ashrrev_i32_e32 v9, 31, v4
	v_lshrrev_b32_e32 v9, 26, v9
	v_add_u32_e32 v9, v4, v9
	v_lshlrev_b32_e32 v8, 3, v5
	v_ashrrev_i32_e32 v10, 6, v9
	v_and_b32_e32 v9, 0xc0, v9
	v_and_b32_e32 v8, -16, v8
	v_lshlrev_b32_e32 v5, 5, v5
	v_sub_u32_e32 v4, v4, v9
	v_add_u32_e32 v8, v10, v8
	v_and_b32_e32 v5, 32, v5
	v_ashrrev_i16_sdwa v4, v198, sext(v4) dst_sel:DWORD dst_unused:UNUSED_PAD src0_sel:DWORD src1_sel:BYTE_0
	v_and_b32_e32 v10, 3, v10
	s_ff1_i32_b32 s52, vcc_lo
	v_add_u32_sdwa v4, v5, sext(v4) dst_sel:DWORD dst_unused:UNUSED_PAD src0_sel:DWORD src1_sel:WORD_0
	v_lshlrev_b32_e32 v5, 1, v8
	v_lshrrev_b32_e32 v9, 2, v8
	v_and_or_b32 v10, v8, s1, v10
	s_lshl_b32 s1, s52, 2
	v_and_b32_e32 v5, 24, v5
	v_and_b32_e32 v9, 4, v9
	s_add_i32 s1, s1, 0
	v_or3_b32 v5, v10, v9, v5
	v_lshlrev_b32_e32 v9, 1, v4
	s_add_i32 s12, s1, 0x20200
	v_lshl_add_u32 v201, v5, 11, v9
	v_mov_b32_e32 v5, s12
	ds_read_b32 v5, v5
	s_add_i32 s1, s1, 0x20100
	s_lshr_b32 s3, s2, 6
	s_lshr_b32 s4, s2, 8
	s_lshl_b32 s5, s3, 10
	s_waitcnt lgkmcnt(0)
	v_readfirstlane_b32 s12, v5
	v_mov_b32_e32 v5, s1
	ds_read_b32 v5, v5
	s_sub_i32 s0, s0, s12
	s_abs_i32 s13, s0
	v_lshrrev_b32_e32 v3, 10, v3
	v_lshrrev_b32_e32 v4, 10, v4
	s_waitcnt lgkmcnt(0)
	v_readfirstlane_b32 s1, v5
	s_addk_i32 s1, 0xff
	s_ashr_i32 s1, s1, 8
	s_abs_i32 s14, s1
	v_cvt_f32_u32_e32 v10, s14
	s_sub_i32 s16, 0, s14
	s_xor_b32 s12, s0, s1
	s_ashr_i32 s12, s12, 31
	v_rcp_iflag_f32_e32 v10, v10
	v_add_u32_e32 v3, v3, v6
	v_add_u32_e32 v4, v4, v8
	v_and_b32_e32 v3, 0x1fffff, v3
	v_mul_f32_e32 v10, 0x4f7ffffe, v10
	v_cvt_u32_f32_e32 v10, v10
	v_and_b32_e32 v4, 0x1fffff, v4
	v_add_u32_e32 v5, -1, v5
	v_and_b32_e32 v202, 0x7fe, v7
	v_readfirstlane_b32 s17, v10
	s_mul_i32 s16, s16, s17
	s_mul_hi_u32 s16, s17, s16
	s_add_i32 s17, s17, s16
	s_mul_hi_u32 s16, s13, s17
	s_mul_i32 s17, s16, s14
	s_sub_i32 s13, s13, s17
	s_add_i32 s17, s16, 1
	s_sub_i32 s22, s13, s14
	s_cmp_ge_u32 s13, s14
	s_cselect_b32 s16, s17, s16
	s_cselect_b32 s13, s22, s13
	s_add_i32 s17, s16, 1
	s_cmp_ge_u32 s13, s14
	s_cselect_b32 s13, s17, s16
	s_xor_b32 s13, s13, s12
	s_sub_i32 s54, s13, s12
	s_mul_i32 s1, s1, s54
	s_sub_i32 s79, s0, s1
	s_lshl_b32 s0, s79, 8
	v_add_u32_e32 v6, s0, v3
	v_add_u32_e32 v8, s0, v4
	s_bitset1_b32 s0, 7
	v_add_u32_e32 v10, s0, v3
	v_add_u32_e32 v11, s0, v4
	s_lshl_b32 s0, s52, 15
	s_add_u32 s0, s83, s0
	v_min_i32_e32 v6, v6, v5
	v_min_i32_e32 v8, v8, v5
	v_min_i32_e32 v10, v10, v5
	v_min_i32_e32 v5, v11, v5
	s_addc_u32 s1, s86, 0
	s_ashr_i32 s55, s54, 31
	v_lshlrev_b32_e32 v6, 2, v6
	v_lshlrev_b32_e32 v8, 2, v8
	v_lshlrev_b32_e32 v10, 2, v10
	v_lshlrev_b32_e32 v5, 2, v5
	global_load_dword v11, v6, s[0:1]
	global_load_dword v12, v8, s[0:1]
	global_load_dword v13, v10, s[0:1]
	global_load_dword v14, v5, s[0:1]
	s_lshl_b32 s12, s52, 23
	s_lshl_b64 s[0:1], s[54:55], 19
	s_add_u32 s12, s81, s12
	s_addc_u32 s13, s82, 0
	s_add_u32 s58, s12, s0
	s_addc_u32 s59, s13, s1
	s_add_i32 s29, s5, 0
	s_add_i32 s30, s29, 0x10000
	s_mov_b32 s0, m0
	s_mov_b32 m0, s30
	s_nop 0
	global_load_lds_dwordx4 v194, s[58:59]
	s_mov_b32 m0, s0
	s_add_i32 s31, s29, 0x12000
	s_mov_b32 s0, m0
	s_mov_b32 m0, s31
	s_nop 0
	global_load_lds_dwordx4 v201, s[58:59]
	s_mov_b32 m0, s0
	s_add_u32 s0, s58, 0x40000
	s_addc_u32 s1, s59, 0
	s_add_i32 s36, s29, 0x14000
	s_mov_b32 s5, m0
	s_mov_b32 m0, s36
	s_nop 0
	global_load_lds_dwordx4 v194, s[0:1]
	s_mov_b32 m0, s5
	s_add_i32 s55, s29, 0x16000
	s_mov_b32 s5, m0
	s_mov_b32 m0, s55
	s_nop 0
	global_load_lds_dwordx4 v201, s[0:1]
	s_mov_b32 m0, s5
	s_waitcnt vmcnt(4)
	v_lshl_or_b32 v204, v11, 11, v202
	v_and_b32_e32 v203, 0x7fe, v9
	s_mov_b32 s0, m0
	s_mov_b32 m0, s29
	s_nop 0
	global_load_lds_dwordx4 v204, s[18:19]
	s_mov_b32 m0, s0
	v_lshl_or_b32 v205, v12, 11, v203
	s_add_i32 s85, s29, 0x2000
	s_mov_b32 s0, m0
	s_mov_b32 m0, s85
	s_nop 0
	global_load_lds_dwordx4 v205, s[18:19]
	s_mov_b32 m0, s0
	v_lshl_or_b32 v206, v13, 11, v202
	s_add_i32 s16, s29, 0x4000
	s_mov_b32 s0, m0
	s_mov_b32 m0, s16
	s_nop 0
	global_load_lds_dwordx4 v206, s[18:19]
	s_mov_b32 m0, s0
	v_lshl_or_b32 v207, v14, 11, v203
	s_add_i32 s17, s29, 0x6000
	s_mov_b32 s0, m0
	s_mov_b32 m0, s17
	s_nop 0
	global_load_lds_dwordx4 v207, s[18:19]
	s_mov_b32 m0, s0
	s_cmp_eq_u32 s4, 1
	s_cselect_b64 s[0:1], -1, 0
	s_cmp_lg_u32 s4, 1
	s_cbranch_scc1 .LBB0_999
	s_barrier

; __device__ __forceinline__ int fresh_lane() { int l = (int)__builtin_amdgcn_mbcnt_hi(~0u, __builtin_amdgcn_mbcnt_lo(~0u, 0u)); asm volatile("" : "+v"(l)); return l; }
;     __device__ __forceinline__ bool next(int i, Unit& u) const {
;         if (i >= hi) return false;
;         const int L = i * G + c;
;         const unsigned msk = (unsigned)__ballot(L < pfxU[(fresh_lane() & 31) + 1]);
;         if (msk == 0u) return false;
;         const int e = __builtin_ctz(msk);
;         const int r = L - __builtin_amdgcn_readfirstlane(pfxU[e]), mt = (__builtin_amdgcn_readfirstlane(cnt[e]) + 255) >> 8;
;         u.e = e; u.pn = r / mt; u.pm = r - u.pn * mt; return true;
; template <class Epi, class Sched>
; __device__ __forceinline__ void gemm_phase(LAS unsigned char* lds, const Sched& S, const Epi& E) {
;     ...
;     for (;;) {
;         const bool has_next = S.next(ui + 1, nxt);
.LBB0_1002:
	s_add_i32 s25, s25, 1
	s_cmp_ge_i32 s25, s87
	s_mov_b64 s[56:57], 0
	s_cbranch_scc1 .LBB0_1005
	v_mov_b32_e32 v2, v1
	s_mul_i32 s2, s25, s33
	v_and_b32_e32 v2, 31, v2
	v_lshl_add_u32 v2, v2, 2, s97
	ds_read_b32 v2, v2 offset:4
	v_readlane_b32 s3, v252, 50
	s_add_i32 s2, s2, s3
	s_waitcnt lgkmcnt(0)
	v_cmp_lt_i32_e32 vcc, s2, v2
	s_cmp_eq_u32 vcc_lo, 0
	s_cbranch_scc1 .LBB0_1005
	s_ff1_i32_b32 s40, vcc_lo
	s_lshl_b32 s3, s40, 2
	s_add_i32 s3, s3, 0
	s_add_i32 s12, s3, 0x20200
	v_mov_b32_e32 v2, s12
	ds_read_b32 v2, v2
	s_add_i32 s3, s3, 0x20100
	s_mov_b64 s[56:57], -1
	s_waitcnt lgkmcnt(0)
	v_readfirstlane_b32 s12, v2
	v_mov_b32_e32 v2, s3
	ds_read_b32 v2, v2
	s_sub_i32 s2, s2, s12
	s_abs_i32 s13, s2
	s_waitcnt lgkmcnt(0)
	v_readfirstlane_b32 s3, v2
	s_addk_i32 s3, 0xff
	s_ashr_i32 s3, s3, 8
	s_abs_i32 s41, s3
	v_cvt_f32_u32_e32 v2, s41
	s_sub_i32 s42, 0, s41
	s_xor_b32 s12, s2, s3
	s_ashr_i32 s12, s12, 31
	v_rcp_iflag_f32_e32 v2, v2
	s_nop 0
	v_mul_f32_e32 v2, 0x4f7ffffe, v2
	v_cvt_u32_f32_e32 v2, v2
	s_nop 0
	v_readfirstlane_b32 s43, v2
	s_mul_i32 s42, s42, s43
	s_mul_hi_u32 s42, s43, s42
	s_add_i32 s43, s43, s42
	s_mul_hi_u32 s42, s13, s43
	s_mul_i32 s43, s42, s41
	s_sub_i32 s13, s13, s43
	s_add_i32 s43, s42, 1
	s_sub_i32 s44, s13, s41
	s_cmp_ge_u32 s13, s41
	s_cselect_b32 s42, s43, s42
	s_cselect_b32 s13, s44, s13
	s_add_i32 s43, s42, 1
	s_cmp_ge_u32 s13, s41
	s_cselect_b32 s13, s43, s42
	s_xor_b32 s13, s13, s12
	s_sub_i32 s42, s13, s12
	s_mul_i32 s3, s3, s42
	s_sub_i32 s84, s2, s3

; __global__ void __launch_bounds__(NT, 2) mk_fwd(Args args) {
	.amdhsa_kernel _Z6mk_fwd4Args
		.amdhsa_group_segment_fixed_size 0
		.amdhsa_private_segment_fixed_size 0
		.amdhsa_kernarg_size 424
		.amdhsa_user_sgpr_count 2
		.amdhsa_user_sgpr_dispatch_ptr 0
		.amdhsa_user_sgpr_queue_ptr 0
		.amdhsa_user_sgpr_kernarg_segment_ptr 1
		.amdhsa_user_sgpr_dispatch_id 0
		.amdhsa_user_sgpr_kernarg_preload_length 0
		.amdhsa_user_sgpr_kernarg_preload_offset 0
		.amdhsa_user_sgpr_private_segment_size 0
		.amdhsa_uses_dynamic_stack 0
		.amdhsa_enable_private_segment 0
		.amdhsa_system_sgpr_workgroup_id_x 1
		.amdhsa_system_sgpr_workgroup_id_y 0
		.amdhsa_system_sgpr_workgroup_id_z 0
		.amdhsa_system_sgpr_workgroup_info 0
		.amdhsa_system_vgpr_workitem_id 0
		.amdhsa_next_free_vgpr 254
		.amdhsa_next_free_sgpr 102
		.amdhsa_accum_offset 256
		.amdhsa_reserve_vcc 1
		.amdhsa_float_round_mode_32 0
		.amdhsa_float_round_mode_16_64 0
		.amdhsa_float_denorm_mode_32 3
		.amdhsa_float_denorm_mode_16_64 3
		.amdhsa_dx10_clamp 1
		.amdhsa_ieee_mode 1
		.amdhsa_fp16_overflow 0
		.amdhsa_tg_split 0
		.amdhsa_exception_fp_ieee_invalid_op 0
		.amdhsa_exception_fp_denorm_src 0
		.amdhsa_exception_fp_ieee_div_zero 0
		.amdhsa_exception_fp_ieee_overflow 0
		.amdhsa_exception_fp_ieee_underflow 0
		.amdhsa_exception_fp_ieee_inexact 0
		.amdhsa_exception_int_div_zero 0
	.end_amdhsa_kernel

; __global__ void __launch_bounds__(NT, 2) mk_fwd(Args args) {
amdhsa.kernels:
  - .agpr_count:     0
    .args:
      - .offset:         0
        .size:           168
        .value_kind:     by_value
      - .offset:         168
        .size:           4
        .value_kind:     hidden_block_count_x
      - .offset:         172
        .size:           4
        .value_kind:     hidden_block_count_y
      - .offset:         176
        .size:           4
        .value_kind:     hidden_block_count_z
      - .offset:         180
        .size:           2
        .value_kind:     hidden_group_size_x
      - .offset:         182
        .size:           2
        .value_kind:     hidden_group_size_y
      - .offset:         184
        .size:           2
        .value_kind:     hidden_group_size_z
      - .offset:         186
        .size:           2
        .value_kind:     hidden_remainder_x
      - .offset:         188
        .size:           2
        .value_kind:     hidden_remainder_y
      - .offset:         190
        .size:           2
        .value_kind:     hidden_remainder_z
      - .offset:         208
        .size:           8
        .value_kind:     hidden_global_offset_x
      - .offset:         216
        .size:           8
        .value_kind:     hidden_global_offset_y
      - .offset:         224
        .size:           8
        .value_kind:     hidden_global_offset_z
      - .offset:         232
        .size:           2
        .value_kind:     hidden_grid_dims
      - .offset:         288
        .size:           4
        .value_kind:     hidden_dynamic_lds_size
    .group_segment_fixed_size: 0
    .kernarg_segment_align: 8
    .kernarg_segment_size: 424
    .language:       OpenCL C
    .language_version:
      - 2
      - 0
    .max_flat_workgroup_size: 512
    .name:           _Z6mk_fwd4Args
    .private_segment_fixed_size: 0
    .sgpr_count:     108
    .sgpr_spill_count: 180
    .symbol:         _Z6mk_fwd4Args.kd
    .uniform_work_group_size: 1
    .uses_dynamic_stack: false
    .vgpr_count:     254
    .vgpr_spill_count: 0
    .wavefront_size: 64
